# out_kernel: chunk c fragment reads now overlap staging of chunk c+1 into the other LDS buffer before the MFMAs (one barrier per chunk kept)
# speedup vs baseline: 1.0022x; 1.0022x over previous
_Z10out_kernelPKDF16_S0_PKfPf:
	s_load_dwordx8 s[4:11], s[0:1], 0x0
	s_lshr_b32 s12, s2, 3
	s_and_b32 s13, s2, 7
	s_lshl_b32 s14, s12, 5
	s_lshl_b32 s15, s13, 6
	v_lshrrev_b32_e32 v1, 3, v0
	v_and_b32_e32 v2, 7, v0
	v_lshlrev_b32_e32 v4, 4, v2
	v_add_u32_e32 v3, s14, v1
	v_lshl_or_b32 v3, v3, 10, v4
	v_add_u32_e32 v5, s15, v1
	v_lshl_or_b32 v5, v5, 10, v4
	v_add_u32_e32 v6, 0x8000, v5
	v_mul_u32_u24_e32 v7, 0x90, v1
	v_add_u32_e32 v7, v7, v4
	v_and_b32_e32 v8, 15, v0
	v_and_b32_e32 v9, 48, v0
	v_lshrrev_b32_e32 v10, 6, v0
	v_mul_u32_u24_e32 v11, 0x90, v8
	v_add_u32_e32 v11, v11, v9
	v_mul_u32_u24_e32 v12, 0x900, v10
	v_add_u32_e32 v12, v12, v11
	v_lshl_add_u32 v14, v10, 4, v8
	v_add_u32_e32 v14, s15, v14
	v_lshlrev_b32_e32 v15, 2, v14
	v_lshrrev_b32_e32 v13, 2, v9
	v_add_u32_e32 v13, s14, v13
	v_lshl_add_u32 v13, v13, 9, v14
	v_lshlrev_b32_e32 v16, 2, v13
	v_add_u32_e32 v17, 0x1000, v16
	v_add_u32_e32 v18, 0x8000, v16
	v_add_u32_e32 v19, 0x9000, v16
	s_waitcnt lgkmcnt(0)
	global_load_dwordx4 v[24:27], v3, s[4:5]
	global_load_dwordx4 v[28:31], v5, s[6:7]
	global_load_dwordx4 v[32:35], v6, s[6:7]
	global_load_dwordx4 v[36:39], v3, s[4:5] offset:128
	global_load_dwordx4 v[40:43], v5, s[6:7] offset:128
	global_load_dwordx4 v[44:47], v6, s[6:7] offset:128
	global_load_dwordx4 v[48:51], v3, s[4:5] offset:256
	global_load_dwordx4 v[52:55], v5, s[6:7] offset:256
	global_load_dwordx4 v[56:59], v6, s[6:7] offset:256
	global_load_dword v20, v15, s[8:9]
	s_waitcnt vmcnt(7)
	ds_write_b128 v7, v[24:27] offset:18432
	ds_write_b128 v7, v[28:31]
	ds_write_b128 v7, v[32:35] offset:4608
	global_load_dwordx4 v[24:27], v3, s[4:5] offset:384
	global_load_dwordx4 v[28:31], v5, s[6:7] offset:384
	global_load_dwordx4 v[32:35], v6, s[6:7] offset:384
	s_waitcnt lgkmcnt(0)
	s_barrier
	ds_read_b128 v[60:63], v11 offset:18432
	ds_read_b128 v[76:79], v12
	ds_read_b128 v[68:71], v11 offset:20736
	ds_read_b128 v[64:67], v11 offset:18496
	ds_read_b128 v[80:83], v12 offset:64
	ds_read_b128 v[72:75], v11 offset:20800
	s_waitcnt vmcnt(7)
	ds_write_b128 v7, v[36:39] offset:23040
	ds_write_b128 v7, v[40:43] offset:9216
	ds_write_b128 v7, v[44:47] offset:13824
	global_load_dwordx4 v[36:39], v3, s[4:5] offset:512
	global_load_dwordx4 v[40:43], v5, s[6:7] offset:512
	global_load_dwordx4 v[44:47], v6, s[6:7] offset:512
	s_waitcnt lgkmcnt(7)
	v_mfma_f32_16x16x32_f16 a[0:3], v[60:63], v[76:79], 0
	s_waitcnt lgkmcnt(6)
	v_mfma_f32_16x16x32_f16 a[4:7], v[68:71], v[76:79], 0
	s_waitcnt lgkmcnt(4)
	v_mfma_f32_16x16x32_f16 a[0:3], v[64:67], v[80:83], a[0:3]
	s_waitcnt lgkmcnt(3)
	v_mfma_f32_16x16x32_f16 a[4:7], v[72:75], v[80:83], a[4:7]
	s_waitcnt lgkmcnt(0)
	s_barrier
	ds_read_b128 v[60:63], v11 offset:23040
	ds_read_b128 v[76:79], v12 offset:9216
	ds_read_b128 v[68:71], v11 offset:25344
	ds_read_b128 v[64:67], v11 offset:23104
	ds_read_b128 v[80:83], v12 offset:9280
	ds_read_b128 v[72:75], v11 offset:25408
	s_waitcnt vmcnt(7)
	ds_write_b128 v7, v[48:51] offset:18432
	ds_write_b128 v7, v[52:55]
	ds_write_b128 v7, v[56:59] offset:4608
	global_load_dwordx4 v[48:51], v3, s[4:5] offset:640
	global_load_dwordx4 v[52:55], v5, s[6:7] offset:640
	global_load_dwordx4 v[56:59], v6, s[6:7] offset:640
	s_waitcnt lgkmcnt(7)
	v_mfma_f32_16x16x32_f16 a[0:3], v[60:63], v[76:79], a[0:3]
	s_waitcnt lgkmcnt(6)
	v_mfma_f32_16x16x32_f16 a[4:7], v[68:71], v[76:79], a[4:7]
	s_waitcnt lgkmcnt(4)
	v_mfma_f32_16x16x32_f16 a[0:3], v[64:67], v[80:83], a[0:3]
	s_waitcnt lgkmcnt(3)
	v_mfma_f32_16x16x32_f16 a[4:7], v[72:75], v[80:83], a[4:7]
	s_waitcnt lgkmcnt(0)
	s_barrier
	ds_read_b128 v[60:63], v11 offset:18432
	ds_read_b128 v[76:79], v12
	ds_read_b128 v[68:71], v11 offset:20736
	ds_read_b128 v[64:67], v11 offset:18496
	ds_read_b128 v[80:83], v12 offset:64
	ds_read_b128 v[72:75], v11 offset:20800
	s_waitcnt vmcnt(6)
	ds_write_b128 v7, v[24:27] offset:23040
	ds_write_b128 v7, v[28:31] offset:9216
	ds_write_b128 v7, v[32:35] offset:13824
	global_load_dwordx4 v[24:27], v3, s[4:5] offset:768
	global_load_dwordx4 v[28:31], v5, s[6:7] offset:768
	global_load_dwordx4 v[32:35], v6, s[6:7] offset:768
	s_waitcnt lgkmcnt(7)
	v_mfma_f32_16x16x32_f16 a[0:3], v[60:63], v[76:79], a[0:3]
	s_waitcnt lgkmcnt(6)
	v_mfma_f32_16x16x32_f16 a[4:7], v[68:71], v[76:79], a[4:7]
	s_waitcnt lgkmcnt(4)
	v_mfma_f32_16x16x32_f16 a[0:3], v[64:67], v[80:83], a[0:3]
	s_waitcnt lgkmcnt(3)
	v_mfma_f32_16x16x32_f16 a[4:7], v[72:75], v[80:83], a[4:7]
	s_waitcnt lgkmcnt(0)
	s_barrier
	ds_read_b128 v[60:63], v11 offset:23040
	ds_read_b128 v[76:79], v12 offset:9216
	ds_read_b128 v[68:71], v11 offset:25344
	ds_read_b128 v[64:67], v11 offset:23104
	ds_read_b128 v[80:83], v12 offset:9280
	ds_read_b128 v[72:75], v11 offset:25408
	s_waitcnt vmcnt(6)
	ds_write_b128 v7, v[36:39] offset:18432
	ds_write_b128 v7, v[40:43]
	ds_write_b128 v7, v[44:47] offset:4608
	global_load_dwordx4 v[36:39], v3, s[4:5] offset:896
	global_load_dwordx4 v[40:43], v5, s[6:7] offset:896
	global_load_dwordx4 v[44:47], v6, s[6:7] offset:896
	s_waitcnt lgkmcnt(7)
	v_mfma_f32_16x16x32_f16 a[0:3], v[60:63], v[76:79], a[0:3]
	s_waitcnt lgkmcnt(6)
	v_mfma_f32_16x16x32_f16 a[4:7], v[68:71], v[76:79], a[4:7]
	s_waitcnt lgkmcnt(4)
	v_mfma_f32_16x16x32_f16 a[0:3], v[64:67], v[80:83], a[0:3]
	s_waitcnt lgkmcnt(3)
	v_mfma_f32_16x16x32_f16 a[4:7], v[72:75], v[80:83], a[4:7]
	s_waitcnt lgkmcnt(0)
	s_barrier
	ds_read_b128 v[60:63], v11 offset:18432
	ds_read_b128 v[76:79], v12
	ds_read_b128 v[68:71], v11 offset:20736
	ds_read_b128 v[64:67], v11 offset:18496
	ds_read_b128 v[80:83], v12 offset:64
	ds_read_b128 v[72:75], v11 offset:20800
	s_waitcnt vmcnt(6)
	ds_write_b128 v7, v[48:51] offset:23040
	ds_write_b128 v7, v[52:55] offset:9216
	ds_write_b128 v7, v[56:59] offset:13824
	s_waitcnt lgkmcnt(7)
	v_mfma_f32_16x16x32_f16 a[0:3], v[60:63], v[76:79], a[0:3]
	s_waitcnt lgkmcnt(6)
	v_mfma_f32_16x16x32_f16 a[4:7], v[68:71], v[76:79], a[4:7]
	s_waitcnt lgkmcnt(4)
	v_mfma_f32_16x16x32_f16 a[0:3], v[64:67], v[80:83], a[0:3]
	s_waitcnt lgkmcnt(3)
	v_mfma_f32_16x16x32_f16 a[4:7], v[72:75], v[80:83], a[4:7]
	s_waitcnt lgkmcnt(0)
	s_barrier
	ds_read_b128 v[60:63], v11 offset:23040
	ds_read_b128 v[76:79], v12 offset:9216
	ds_read_b128 v[68:71], v11 offset:25344
	ds_read_b128 v[64:67], v11 offset:23104
	ds_read_b128 v[80:83], v12 offset:9280
	ds_read_b128 v[72:75], v11 offset:25408
	s_waitcnt vmcnt(3)
	ds_write_b128 v7, v[24:27] offset:18432
	ds_write_b128 v7, v[28:31]
	ds_write_b128 v7, v[32:35] offset:4608
	s_waitcnt lgkmcnt(7)
	v_mfma_f32_16x16x32_f16 a[0:3], v[60:63], v[76:79], a[0:3]
	s_waitcnt lgkmcnt(6)
	v_mfma_f32_16x16x32_f16 a[4:7], v[68:71], v[76:79], a[4:7]
	s_waitcnt lgkmcnt(4)
	v_mfma_f32_16x16x32_f16 a[0:3], v[64:67], v[80:83], a[0:3]
	s_waitcnt lgkmcnt(3)
	v_mfma_f32_16x16x32_f16 a[4:7], v[72:75], v[80:83], a[4:7]
	s_waitcnt lgkmcnt(0)
	s_barrier
	ds_read_b128 v[60:63], v11 offset:18432
	ds_read_b128 v[76:79], v12
	ds_read_b128 v[68:71], v11 offset:20736
	ds_read_b128 v[64:67], v11 offset:18496
	ds_read_b128 v[80:83], v12 offset:64
	ds_read_b128 v[72:75], v11 offset:20800
	s_waitcnt vmcnt(0)
	ds_write_b128 v7, v[36:39] offset:23040
	ds_write_b128 v7, v[40:43] offset:9216
	ds_write_b128 v7, v[44:47] offset:13824
	s_waitcnt lgkmcnt(7)
	v_mfma_f32_16x16x32_f16 a[0:3], v[60:63], v[76:79], a[0:3]
	s_waitcnt lgkmcnt(6)
	v_mfma_f32_16x16x32_f16 a[4:7], v[68:71], v[76:79], a[4:7]
	s_waitcnt lgkmcnt(4)
	v_mfma_f32_16x16x32_f16 a[0:3], v[64:67], v[80:83], a[0:3]
	s_waitcnt lgkmcnt(3)
	v_mfma_f32_16x16x32_f16 a[4:7], v[72:75], v[80:83], a[4:7]
	s_waitcnt lgkmcnt(0)
	s_barrier
	ds_read_b128 v[60:63], v11 offset:23040
	ds_read_b128 v[76:79], v12 offset:9216
	ds_read_b128 v[68:71], v11 offset:25344
	ds_read_b128 v[64:67], v11 offset:23104
	ds_read_b128 v[80:83], v12 offset:9280
	ds_read_b128 v[72:75], v11 offset:25408
	s_waitcnt lgkmcnt(4)
	v_mfma_f32_16x16x32_f16 a[0:3], v[60:63], v[76:79], a[0:3]
	s_waitcnt lgkmcnt(3)
	v_mfma_f32_16x16x32_f16 a[4:7], v[68:71], v[76:79], a[4:7]
	s_waitcnt lgkmcnt(1)
	v_mfma_f32_16x16x32_f16 a[0:3], v[64:67], v[80:83], a[0:3]
	s_waitcnt lgkmcnt(0)
	v_mfma_f32_16x16x32_f16 a[4:7], v[72:75], v[80:83], a[4:7]
	s_nop 7
	v_accvgpr_read_b32 v60, a0
	v_accvgpr_read_b32 v61, a1
	v_accvgpr_read_b32 v62, a2
	v_accvgpr_read_b32 v63, a3
	v_accvgpr_read_b32 v64, a4
	v_accvgpr_read_b32 v65, a5
	v_accvgpr_read_b32 v66, a6
	v_accvgpr_read_b32 v67, a7
	v_add_f32_e32 v60, v20, v60
	v_add_f32_e32 v61, v20, v61
	v_add_f32_e32 v62, v20, v62
	v_add_f32_e32 v63, v20, v63
	v_add_f32_e32 v64, v20, v64
	v_add_f32_e32 v65, v20, v65
	v_add_f32_e32 v66, v20, v66
	v_add_f32_e32 v67, v20, v67
	global_store_dword v16, v60, s[10:11]
	global_store_dword v16, v61, s[10:11] offset:2048
	global_store_dword v17, v62, s[10:11]
	global_store_dword v17, v63, s[10:11] offset:2048
	global_store_dword v18, v64, s[10:11]
	global_store_dword v18, v65, s[10:11] offset:2048
	global_store_dword v19, v66, s[10:11]
	global_store_dword v19, v67, s[10:11] offset:2048
	s_endpgm
